# baseline (speedup 1.0000x reference)
_Z12final_kernelPKfS0_Pfi:
	s_load_dwordx2 s[2:3], s[0:1], 0x8
	s_load_dwordx2 s[14:15], s[0:1], 0x0
	s_load_dwordx2 s[16:17], s[0:1], 0x10
	s_load_dword s13, s[0:1], 0x18
	v_and_b32_e32 v35, 63, v0
	v_lshlrev_b32_e32 v35, 2, v35
	v_lshlrev_b32_e32 v1, 4, v0
	v_or_b32_e32 v34, 0x400, v0
	v_or_b32_e32 v33, 0x800, v0
	v_lshlrev_b32_e32 v2, 4, v34
	s_waitcnt lgkmcnt(0)
	global_load_dword v35, v35, s[14:15]
	global_load_dwordx4 v[26:29], v1, s[2:3]
	global_load_dwordx4 v[22:25], v2, s[2:3]
	v_lshlrev_b32_e32 v1, 4, v33
	v_or_b32_e32 v32, 0xc00, v0
	v_or_b32_e32 v31, 0x1000, v0
	v_lshlrev_b32_e32 v2, 4, v32
	global_load_dwordx4 v[18:21], v1, s[2:3]
	global_load_dwordx4 v[14:17], v2, s[2:3]
	v_lshlrev_b32_e32 v1, 4, v31
	v_or_b32_e32 v30, 0x1400, v0
	v_lshlrev_b32_e32 v2, 4, v30
	global_load_dwordx4 v[10:13], v1, s[2:3]
	global_load_dwordx4 v[6:9], v2, s[2:3]
	v_or_b32_e32 v1, 0x1800, v0
	s_movk_i32 s4, 0x1940
	v_cmp_gt_u32_e32 vcc, s4, v1
	s_and_saveexec_b64 s[4:5], vcc
	s_cbranch_execz .LBB1_2
	v_lshlrev_b32_e32 v2, 4, v1
	global_load_dwordx4 v[2:5], v2, s[2:3]

.LBB1_14:
	s_or_b64 exec, exec, s[6:7]
	v_mov_b32_e32 v3, 0
	s_mov_b32 s6, s13
	s_waitcnt lgkmcnt(0)
	s_barrier
	ds_read_b32 v1, v3 offset:26112
	s_movk_i32 s7, 0x194
	v_lshlrev_b32_e32 v2, 2, v0
	v_cmp_gt_u32_e32 vcc, 0x100, v0
	s_mov_b64 s[36:37], vcc
	s_add_u32 s20, s4, 0x1000
	s_addc_u32 s21, s5, 0
	s_add_u32 s22, s4, 0x2000
	s_addc_u32 s23, s5, 0
	s_add_u32 s24, s4, 0x3000
	s_addc_u32 s25, s5, 0
	s_add_u32 s26, s4, 0x4000
	s_addc_u32 s27, s5, 0
	s_add_u32 s28, s4, 0x5000
	s_addc_u32 s29, s5, 0
	s_add_u32 s30, s4, 0x6000
	s_addc_u32 s31, s5, 0
	v_lshrrev_b32_e32 v5, 2, v0
	v_mul_u32_u24_e32 v5, 0x147b, v5
	v_lshrrev_b32_e32 v5, 17, v5
	v_mul_u32_u24_e32 v6, 0x64, v5
	v_sub_u32_e32 v17, v0, v6
	v_lshlrev_b32_e32 v6, 2, v17
	v_mad_u32_u24 v6, v5, s7, v6
	ds_read_b32 v10, v6
	v_add_u32_e32 v4, 0x400, v0
	v_lshrrev_b32_e32 v5, 2, v4
	v_mul_u32_u24_e32 v5, 0x147b, v5
	v_lshrrev_b32_e32 v5, 17, v5
	v_mul_u32_u24_e32 v6, 0x64, v5
	v_sub_u32_e32 v18, v4, v6
	v_lshlrev_b32_e32 v6, 2, v18
	v_mad_u32_u24 v6, v5, s7, v6
	ds_read_b32 v11, v6
	v_add_u32_e32 v4, 0x800, v0
	v_lshrrev_b32_e32 v5, 2, v4
	v_mul_u32_u24_e32 v5, 0x147b, v5
	v_lshrrev_b32_e32 v5, 17, v5
	v_mul_u32_u24_e32 v6, 0x64, v5
	v_sub_u32_e32 v19, v4, v6
	v_lshlrev_b32_e32 v6, 2, v19
	v_mad_u32_u24 v6, v5, s7, v6
	ds_read_b32 v12, v6
	v_add_u32_e32 v4, 0xc00, v0
	v_lshrrev_b32_e32 v5, 2, v4
	v_mul_u32_u24_e32 v5, 0x147b, v5
	v_lshrrev_b32_e32 v5, 17, v5
	v_mul_u32_u24_e32 v6, 0x64, v5
	v_sub_u32_e32 v20, v4, v6
	v_lshlrev_b32_e32 v6, 2, v20
	v_mad_u32_u24 v6, v5, s7, v6
	ds_read_b32 v13, v6
	v_add_u32_e32 v4, 0x1000, v0
	v_lshrrev_b32_e32 v5, 2, v4
	v_mul_u32_u24_e32 v5, 0x147b, v5
	v_lshrrev_b32_e32 v5, 17, v5
	v_mul_u32_u24_e32 v6, 0x64, v5
	v_sub_u32_e32 v21, v4, v6
	v_lshlrev_b32_e32 v6, 2, v21
	v_mad_u32_u24 v6, v5, s7, v6
	ds_read_b32 v14, v6
	v_add_u32_e32 v4, 0x1400, v0
	v_lshrrev_b32_e32 v5, 2, v4
	v_mul_u32_u24_e32 v5, 0x147b, v5
	v_lshrrev_b32_e32 v5, 17, v5
	v_mul_u32_u24_e32 v6, 0x64, v5
	v_sub_u32_e32 v22, v4, v6
	v_lshlrev_b32_e32 v6, 2, v22
	v_mad_u32_u24 v6, v5, s7, v6
	ds_read_b32 v15, v6
	v_add_u32_e32 v4, 0x1800, v0
	v_lshrrev_b32_e32 v5, 2, v4
	v_mul_u32_u24_e32 v5, 0x147b, v5
	v_lshrrev_b32_e32 v5, 17, v5
	v_mul_u32_u24_e32 v6, 0x64, v5
	v_sub_u32_e32 v23, v4, v6
	v_lshlrev_b32_e32 v6, 2, v23
	v_mad_u32_u24 v6, v5, s7, v6
	s_and_saveexec_b64 s[38:39], s[36:37]
	ds_read_b32 v16, v6
	s_mov_b64 exec, s[38:39]
	s_waitcnt lgkmcnt(0)
	v_cmp_ge_i32_e32 vcc, v1, v17
	v_cmp_gt_i32_e64 s[0:1], s6, v17
	s_and_b64 s[0:1], vcc, s[0:1]
	v_cndmask_b32_e64 v10, 0, v10, s[0:1]
	v_cmp_ge_i32_e32 vcc, v1, v18
	v_cmp_gt_i32_e64 s[0:1], s6, v18
	s_and_b64 s[0:1], vcc, s[0:1]
	v_cndmask_b32_e64 v11, 0, v11, s[0:1]
	v_cmp_ge_i32_e32 vcc, v1, v19
	v_cmp_gt_i32_e64 s[0:1], s6, v19
	s_and_b64 s[0:1], vcc, s[0:1]
	v_cndmask_b32_e64 v12, 0, v12, s[0:1]
	v_cmp_ge_i32_e32 vcc, v1, v20
	v_cmp_gt_i32_e64 s[0:1], s6, v20
	s_and_b64 s[0:1], vcc, s[0:1]
	v_cndmask_b32_e64 v13, 0, v13, s[0:1]
	v_cmp_ge_i32_e32 vcc, v1, v21
	v_cmp_gt_i32_e64 s[0:1], s6, v21
	s_and_b64 s[0:1], vcc, s[0:1]
	v_cndmask_b32_e64 v14, 0, v14, s[0:1]
	v_cmp_ge_i32_e32 vcc, v1, v22
	v_cmp_gt_i32_e64 s[0:1], s6, v22
	s_and_b64 s[0:1], vcc, s[0:1]
	v_cndmask_b32_e64 v15, 0, v15, s[0:1]
	v_cmp_ge_i32_e32 vcc, v1, v23
	v_cmp_gt_i32_e64 s[0:1], s6, v23
	s_and_b64 s[0:1], vcc, s[0:1]
	v_cndmask_b32_e64 v16, 0, v16, s[0:1]
	global_store_dword v2, v10, s[4:5]
	global_store_dword v2, v11, s[20:21]
	global_store_dword v2, v12, s[22:23]
	global_store_dword v2, v13, s[24:25]
	global_store_dword v2, v14, s[26:27]
	global_store_dword v2, v15, s[28:29]
	s_and_saveexec_b64 s[38:39], s[36:37]
	global_store_dword v2, v16, s[30:31]
	s_endpgm
